# ATT0 tile loop: QK^T MFMAs interleaved with softmax-finish VALU and P.V MFMAs with softmax-start VALU inside each wave (register renames only, same instructions)
# baseline (speedup 1.0000x reference)
.LBB0_503:
	s_add_i32 s36, s19, -3
	s_cmp_lt_u32 s36, s33
	s_cselect_b64 s[6:7], -1, 0
	s_cmp_ge_u32 s36, s33
	ds_read_b128 v[100:103], v185 offset:49152
	ds_read_b128 v[96:99], v184 offset:49152
	ds_read_b128 v[104:107], v184 offset:57344
	ds_read_b128 v[108:111], v186 offset:49152
	ds_read_b128 v[224:227], v188 offset:49152
	ds_read_b128 v[220:223], v187 offset:49152
	ds_read_b128 v[228:231], v187 offset:57344
	ds_read_b128 v[232:235], v189 offset:49152
	v_add_f32_e32 v202, 0, v64
	v_add_f32_e32 v202, v65, v202
	v_add_f32_e32 v202, v66, v202
	v_add_f32_e32 v202, v67, v202
	v_add_f32_e32 v202, v68, v202
	v_add_f32_e32 v202, v69, v202
	v_add_f32_e32 v202, v70, v202
	v_add_f32_e32 v202, v71, v202
	v_add_f32_e32 v202, v72, v202
	v_add_f32_e32 v202, v73, v202
	s_waitcnt lgkmcnt(0)
	v_mfma_f32_32x32x64_f8f6f4 v[112:127], v[96:103], v[128:135], 0
	v_add_f32_e32 v202, v74, v202
	v_add_f32_e32 v202, v75, v202
	v_exp_f32_e32 v80, v80
	v_add_f32_e32 v202, v76, v202
	v_exp_f32_e32 v81, v81
	v_add_f32_e32 v202, v77, v202
	v_exp_f32_e32 v82, v82
	v_add_f32_e32 v202, v78, v202
	v_mfma_f32_32x32x64_f8f6f4 v[96:111], v[104:111], v[128:135], 0
	v_exp_f32_e32 v83, v83
	v_add_f32_e32 v202, v79, v202
	v_exp_f32_e32 v84, v84
	v_add_f32_e32 v202, v80, v202
	v_exp_f32_e32 v85, v85
	v_add_f32_e32 v202, v81, v202
	v_exp_f32_e32 v86, v86
	v_add_f32_e32 v202, v82, v202
	v_mfma_f32_32x32x64_f8f6f4 v[112:127], v[220:227], v[136:143], v[112:127]
	v_exp_f32_e32 v87, v87
	v_add_f32_e32 v202, v83, v202
	v_exp_f32_e32 v88, v88
	v_add_f32_e32 v202, v84, v202
	v_exp_f32_e32 v89, v89
	v_add_f32_e32 v202, v85, v202
	v_exp_f32_e32 v90, v90
	v_add_f32_e32 v202, v86, v202
	v_mfma_f32_32x32x64_f8f6f4 v[96:111], v[228:235], v[136:143], v[96:111]
	v_exp_f32_e32 v91, v91
	v_add_f32_e32 v202, v87, v202
	v_exp_f32_e32 v92, v92
	v_add_f32_e32 v202, v88, v202
	v_exp_f32_e32 v93, v93
	v_add_f32_e32 v202, v89, v202
	v_exp_f32_e32 v94, v94
	v_add_f32_e32 v202, v90, v202
	ds_read_b128 v[224:227], v192 offset:49152
	ds_read_b128 v[220:223], v191 offset:49152
	ds_read_b128 v[228:231], v191 offset:57344
	ds_read_b128 v[232:235], v193 offset:49152
	v_exp_f32_e32 v95, v95
	v_add_f32_e32 v202, v91, v202
	v_add_f32_e32 v202, v92, v202
	v_add_f32_e32 v202, v93, v202
	v_add_f32_e32 v202, v94, v202
	v_add_f32_e32 v202, v95, v202
	v_mov_b32_e32 v203, v202
	s_nop 1
	s_waitcnt lgkmcnt(0)
	v_mfma_f32_32x32x64_f8f6f4 v[112:127], v[220:227], v[144:151], v[112:127]
	v_permlane32_swap_b32_e32 v202, v203
	v_cvt_pk_bf16_f32 v204, v64, v65
	v_cvt_pk_bf16_f32 v205, v66, v67
	v_cvt_pk_bf16_f32 v206, v68, v69
	v_cvt_pk_bf16_f32 v207, v70, v71
	v_cvt_pk_bf16_f32 v208, v72, v73
	v_cvt_pk_bf16_f32 v209, v74, v75
	v_cvt_pk_bf16_f32 v210, v76, v77
	v_cvt_pk_bf16_f32 v211, v78, v79
	v_cvt_pk_bf16_f32 v212, v80, v81
	v_cvt_pk_bf16_f32 v213, v82, v83
	v_mfma_f32_32x32x64_f8f6f4 v[96:111], v[228:235], v[144:151], v[96:111]
	v_cvt_pk_bf16_f32 v214, v84, v85
	v_cvt_pk_bf16_f32 v215, v86, v87
	v_cvt_pk_bf16_f32 v216, v88, v89
	v_cvt_pk_bf16_f32 v217, v90, v91
	v_cvt_pk_bf16_f32 v218, v92, v93
	v_cvt_pk_bf16_f32 v219, v94, v95
	s_nop 0
	v_permlane32_swap_b32_e32 v204, v206
	v_permlane32_swap_b32_e32 v205, v207
	v_permlane32_swap_b32_e32 v208, v210
	v_permlane32_swap_b32_e32 v209, v211
	v_permlane32_swap_b32_e32 v212, v214
	v_permlane32_swap_b32_e32 v213, v215
	v_permlane32_swap_b32_e32 v216, v218
	v_permlane32_swap_b32_e32 v217, v219
	ds_read_b64_tr_b16 v[220:221], v190 offset:0
	ds_read_b64_tr_b16 v[222:223], v190 offset:0x800
	ds_read_b64_tr_b16 v[224:225], v190 offset:0x1000
	ds_read_b64_tr_b16 v[226:227], v190 offset:0x1800
	ds_read_b64_tr_b16 v[228:229], v190 offset:0x2000
	ds_read_b64_tr_b16 v[230:231], v190 offset:0x2800
	ds_read_b64_tr_b16 v[232:233], v190 offset:0x3000
	ds_read_b64_tr_b16 v[234:235], v190 offset:0x3800
	v_max_f32_e32 v200, v113, v113
	v_max_f32_e32 v240, v112, v112
	v_max_f32_e32 v200, v240, v200
	v_max3_f32 v200, v200, v114, v115
	v_max3_f32 v200, v200, v116, v117
	v_max3_f32 v200, v200, v118, v119
	v_max3_f32 v200, v200, v120, v121
	v_max3_f32 v200, v200, v122, v123
	s_waitcnt lgkmcnt(0)
	s_nop 0
	v_mfma_f32_32x32x16_bf16 v[0:15], v[204:207], v[220:223], v[0:15]
	v_max3_f32 v200, v200, v124, v125
	v_max3_f32 v200, v200, v126, v127
	v_max3_f32 v200, v200, v96, v97
	v_max3_f32 v200, v200, v98, v99
	v_max3_f32 v200, v200, v100, v101
	ds_read_b64_tr_b16 v[220:221], v190 offset:0x200
	ds_read_b64_tr_b16 v[222:223], v190 offset:0xa00
	v_mfma_f32_32x32x16_bf16 v[0:15], v[208:211], v[224:227], v[0:15]
	v_max3_f32 v200, v200, v102, v103
	v_max3_f32 v200, v200, v104, v105
	v_max3_f32 v200, v200, v106, v107
	v_max3_f32 v200, v200, v108, v109
	v_max3_f32 v200, v200, v110, v111
	ds_read_b64_tr_b16 v[224:225], v190 offset:0x1200
	ds_read_b64_tr_b16 v[226:227], v190 offset:0x1a00
	v_mfma_f32_32x32x16_bf16 v[0:15], v[212:215], v[228:231], v[0:15]
	v_mov_b32_e32 v240, v200
	s_nop 1
	v_permlane32_swap_b32_e32 v200, v240
	ds_read_b64_tr_b16 v[228:229], v190 offset:0x2200
	ds_read_b64_tr_b16 v[230:231], v190 offset:0x2a00
	ds_read_b64_tr_b16 v[236:237], v190 offset:0x3200
	ds_read_b64_tr_b16 v[238:239], v190 offset:0x3a00
	v_max_f32_e32 v240, v240, v240
	v_max_f32_e32 v200, v200, v200
	v_max_f32_e32 v200, v200, v240
	v_sub_f32_e32 v240, v200, v195
	v_cmp_ge_f32_e32 vcc, s93, v240
	v_max_f32_e32 v240, v195, v195
	v_max_f32_e32 v240, v240, v200
	v_sub_f32_e32 v200, v195, v240
	s_waitcnt lgkmcnt(0)
	v_mfma_f32_32x32x16_bf16 v[0:15], v[216:219], v[232:235], v[0:15]
	v_mul_f32_e32 v200, 0x3dd53b94, v200
	v_exp_f32_e32 v200, v200
	s_cmp_eq_u64 vcc, exec
	s_cselect_b64 s[6:7], -1, 0
	v_mfma_f32_32x32x16_bf16 v[48:63], v[204:207], v[220:223], v[48:63]
	v_cndmask_b32_e64 v200, v200, 1.0, s[6:7]
	v_cmp_gt_f32_e32 vcc, 1.0, v200
	v_cndmask_b32_e64 v195, v240, v195, s[6:7]
	v_mul_f32_e32 v240, 0xbdd53b94, v195
	v_mov_b32_e32 v241, v240
	ds_read_b64_tr_b16 v[220:221], v190 offset:0x400
	ds_read_b64_tr_b16 v[222:223], v190 offset:0xc00
	v_mfma_f32_32x32x16_bf16 v[48:63], v[208:211], v[224:227], v[48:63]
	v_fmamk_f32 v112, v112, 0x3dd53b94, v240
	v_fmamk_f32 v113, v113, 0x3dd53b94, v240
	v_fmamk_f32 v114, v114, 0x3dd53b94, v240
	v_fmamk_f32 v115, v115, 0x3dd53b94, v240
	v_fmamk_f32 v116, v116, 0x3dd53b94, v240
	ds_read_b64_tr_b16 v[224:225], v190 offset:0x1400
	ds_read_b64_tr_b16 v[226:227], v190 offset:0x1c00
	v_mfma_f32_32x32x16_bf16 v[48:63], v[212:215], v[228:231], v[48:63]
	v_fmamk_f32 v117, v117, 0x3dd53b94, v240
	v_fmamk_f32 v118, v118, 0x3dd53b94, v240
	v_fmamk_f32 v119, v119, 0x3dd53b94, v240
	v_fmamk_f32 v120, v120, 0x3dd53b94, v240
	v_fmamk_f32 v121, v121, 0x3dd53b94, v240
	ds_read_b64_tr_b16 v[228:229], v190 offset:0x2400
	ds_read_b64_tr_b16 v[230:231], v190 offset:0x2c00
	ds_read_b64_tr_b16 v[232:233], v190 offset:0x3400
	ds_read_b64_tr_b16 v[234:235], v190 offset:0x3c00
	v_fmamk_f32 v122, v122, 0x3dd53b94, v240
	v_fmamk_f32 v123, v123, 0x3dd53b94, v240
	v_fmamk_f32 v124, v124, 0x3dd53b94, v240
	v_fmamk_f32 v125, v125, 0x3dd53b94, v240
	v_fmamk_f32 v126, v126, 0x3dd53b94, v240
	v_fmac_f32_e32 v241, 0x3dd53b94, v127
	v_exp_f32_e32 v112, v112
	s_waitcnt lgkmcnt(0)
	v_mfma_f32_32x32x16_bf16 v[48:63], v[216:219], v[236:239], v[48:63]
	v_exp_f32_e32 v113, v113
	v_exp_f32_e32 v114, v114
	v_mfma_f32_32x32x16_bf16 v[32:47], v[204:207], v[220:223], v[32:47]
	v_exp_f32_e32 v115, v115
	v_exp_f32_e32 v116, v116
	ds_read_b64_tr_b16 v[220:221], v190 offset:0x600
	ds_read_b64_tr_b16 v[222:223], v190 offset:0xe00
	v_mfma_f32_32x32x16_bf16 v[32:47], v[208:211], v[224:227], v[32:47]
	v_exp_f32_e32 v117, v117
	v_exp_f32_e32 v118, v118
	ds_read_b64_tr_b16 v[224:225], v190 offset:0x1600
	ds_read_b64_tr_b16 v[226:227], v190 offset:0x1e00
	v_mfma_f32_32x32x16_bf16 v[32:47], v[212:215], v[228:231], v[32:47]
	v_exp_f32_e32 v119, v119
	v_exp_f32_e32 v120, v120
	ds_read_b64_tr_b16 v[228:229], v190 offset:0x2600
	ds_read_b64_tr_b16 v[230:231], v190 offset:0x2e00
	ds_read_b64_tr_b16 v[236:237], v190 offset:0x3600
	ds_read_b64_tr_b16 v[238:239], v190 offset:0x3e00
	v_exp_f32_e32 v121, v121
	v_exp_f32_e32 v122, v122
	v_exp_f32_e32 v123, v123
	v_exp_f32_e32 v124, v124
	s_waitcnt lgkmcnt(0)
	v_mfma_f32_32x32x16_bf16 v[32:47], v[216:219], v[232:235], v[32:47]
	v_exp_f32_e32 v125, v125
	v_exp_f32_e32 v126, v126
	v_mfma_f32_32x32x16_bf16 v[16:31], v[204:207], v[220:223], v[16:31]
	v_exp_f32_e32 v127, v241
	v_pk_fma_f32 v[110:111], v[110:111], s[54:55], v[240:241] op_sel_hi:[1,0,0]
	v_mfma_f32_32x32x16_bf16 v[16:31], v[208:211], v[224:227], v[16:31]
	v_pk_fma_f32 v[108:109], v[108:109], s[54:55], v[240:241] op_sel_hi:[1,0,0]
	v_pk_fma_f32 v[106:107], v[106:107], s[54:55], v[240:241] op_sel_hi:[1,0,0]
	v_mfma_f32_32x32x16_bf16 v[16:31], v[212:215], v[228:231], v[16:31]
	v_pk_fma_f32 v[104:105], v[104:105], s[54:55], v[240:241] op_sel_hi:[1,0,0]
	v_pk_fma_f32 v[102:103], v[102:103], s[54:55], v[240:241] op_sel_hi:[1,0,0]
	v_mfma_f32_32x32x16_bf16 v[16:31], v[216:219], v[236:239], v[16:31]
	v_pk_fma_f32 v[100:101], v[100:101], s[54:55], v[240:241] op_sel_hi:[1,0,0]
	v_pk_fma_f32 v[98:99], v[98:99], s[54:55], v[240:241] op_sel_hi:[1,0,0]
	v_pk_fma_f32 v[96:97], v[96:97], s[54:55], v[240:241] op_sel_hi:[1,0,0]
	s_cbranch_vccz .Latt0_nrA
	s_nop 7
	s_nop 7
	s_and_saveexec_b64 s[38:39], s[4:5]
	ds_write_b32 v197, v200 offset:128
	s_or_b64 exec, exec, s[38:39]
	s_waitcnt lgkmcnt(0)
	v_add_u32_e32 v205, s77, v196
	ds_read_b128 v[206:209], v205 offset:224
	ds_read_b128 v[210:213], v205 offset:192
	ds_read_b128 v[214:217], v205 offset:160
	ds_read_b128 v[218:221], v205 offset:128
	s_waitcnt lgkmcnt(0)
	v_pk_mul_f32 v[12:13], v[12:13], v[206:207]
	v_pk_mul_f32 v[8:9], v[8:9], v[210:211]
	v_pk_mul_f32 v[4:5], v[4:5], v[214:215]
	v_pk_mul_f32 v[14:15], v[14:15], v[208:209]
	v_pk_mul_f32 v[10:11], v[10:11], v[212:213]
	v_pk_mul_f32 v[6:7], v[6:7], v[216:217]
	v_pk_mul_f32 v[2:3], v[2:3], v[220:221]
	v_pk_mul_f32 v[0:1], v[0:1], v[218:219]
	v_pk_mul_f32 v[60:61], v[60:61], v[206:207]
	v_pk_mul_f32 v[56:57], v[56:57], v[210:211]
	v_pk_mul_f32 v[52:53], v[52:53], v[214:215]
	v_pk_mul_f32 v[62:63], v[62:63], v[208:209]
	v_pk_mul_f32 v[58:59], v[58:59], v[212:213]
	v_pk_mul_f32 v[54:55], v[54:55], v[216:217]
	v_pk_mul_f32 v[50:51], v[50:51], v[220:221]
	v_pk_mul_f32 v[48:49], v[48:49], v[218:219]
	v_pk_mul_f32 v[44:45], v[44:45], v[206:207]
	v_pk_mul_f32 v[40:41], v[40:41], v[210:211]
	v_pk_mul_f32 v[36:37], v[36:37], v[214:215]
	v_pk_mul_f32 v[46:47], v[46:47], v[208:209]
	v_pk_mul_f32 v[42:43], v[42:43], v[212:213]
	v_pk_mul_f32 v[38:39], v[38:39], v[216:217]
	v_pk_mul_f32 v[34:35], v[34:35], v[220:221]
	v_pk_mul_f32 v[32:33], v[32:33], v[218:219]
	v_pk_mul_f32 v[28:29], v[28:29], v[206:207]
	v_pk_mul_f32 v[24:25], v[24:25], v[210:211]
	v_pk_mul_f32 v[20:21], v[20:21], v[214:215]
	v_pk_mul_f32 v[30:31], v[30:31], v[208:209]
	v_pk_mul_f32 v[26:27], v[26:27], v[212:213]
	v_pk_mul_f32 v[22:23], v[22:23], v[216:217]
	v_pk_mul_f32 v[18:19], v[18:19], v[220:221]
	v_pk_mul_f32 v[16:17], v[16:17], v[218:219]
.Latt0_nrA:
.LBB0_511:
	s_add_i32 s6, s19, -1
	s_min_u32 s36, s6, s42
	s_mul_i32 s6, s36, 0x30000
	s_add_u32 s6, s64, s6
	s_addc_u32 s7, s65, 0
	s_add_i32 s43, s19, -2
	s_mov_b32 m0, s95
	s_waitcnt vmcnt(0)
	v_lshl_add_u64 v[204:205], s[6:7], 0, v[152:153]
	s_cmp_lt_u32 s43, s33
	s_waitcnt lgkmcnt(0)
	s_waitcnt vmcnt(0) lgkmcnt(0)
	s_barrier
	global_load_lds_dwordx4 v[204:205], off
	v_lshl_add_u64 v[204:205], s[6:7], 0, v[154:155]
	s_cselect_b64 s[6:7], -1, 0
	s_min_u32 s38, s43, s42
	s_lshl_b32 s38, s38, 19
	s_add_u32 s38, s66, s38
	s_mov_b32 m0, s18
	s_addc_u32 s39, s67, 0
	global_load_lds_dwordx4 v[204:205], off
	v_lshl_add_u64 v[204:205], s[38:39], 0, v[156:157]
	s_mov_b32 m0, s56
	s_cmp_ge_u32 s43, s33
	global_load_lds_dwordx4 v[204:205], off
	v_lshl_add_u64 v[204:205], s[38:39], 0, v[158:159]
	s_mov_b32 m0, s91
	s_nop 0
	global_load_lds_dwordx4 v[204:205], off
	s_cbranch_scc1 .LBB0_513
	ds_read_b128 v[68:71], v185 offset:32768
	ds_read_b128 v[64:67], v184 offset:32768
	ds_read_b128 v[80:83], v184 offset:40960
	ds_read_b128 v[84:87], v186 offset:32768
	ds_read_b128 v[226:229], v188 offset:32768
	ds_read_b128 v[222:225], v187 offset:32768
	v_add_f32_e32 v204, 0, v112
	v_add_f32_e32 v204, v113, v204
	v_add_f32_e32 v204, v114, v204
	v_add_f32_e32 v204, v115, v204
	v_add_f32_e32 v204, v116, v204
	v_add_f32_e32 v204, v117, v204
	v_add_f32_e32 v204, v118, v204
	v_add_f32_e32 v204, v119, v204
	v_add_f32_e32 v204, v120, v204
	v_add_f32_e32 v204, v121, v204
	s_waitcnt lgkmcnt(0)
	v_mfma_f32_32x32x64_f8f6f4 v[64:79], v[64:71], v[128:135], 0
	v_add_f32_e32 v204, v122, v204
	v_add_f32_e32 v204, v123, v204
	v_exp_f32_e32 v96, v96
	v_add_f32_e32 v204, v124, v204
	v_exp_f32_e32 v97, v97
	v_add_f32_e32 v204, v125, v204
	v_exp_f32_e32 v98, v98
	v_add_f32_e32 v204, v126, v204
	v_mfma_f32_32x32x64_f8f6f4 v[80:95], v[80:87], v[128:135], 0
	v_exp_f32_e32 v99, v99
	v_add_f32_e32 v204, v127, v204
	v_exp_f32_e32 v100, v100
	v_add_f32_e32 v204, v96, v204
	v_exp_f32_e32 v101, v101
	v_add_f32_e32 v204, v97, v204
	v_exp_f32_e32 v102, v102
	v_add_f32_e32 v204, v98, v204
	v_mfma_f32_32x32x64_f8f6f4 v[64:79], v[222:229], v[136:143], v[64:79]
	v_exp_f32_e32 v103, v103
	v_add_f32_e32 v204, v99, v204
	v_exp_f32_e32 v104, v104
	v_add_f32_e32 v204, v100, v204
	v_exp_f32_e32 v105, v105
	v_add_f32_e32 v204, v101, v204
	v_exp_f32_e32 v106, v106
	v_add_f32_e32 v204, v102, v204
	ds_read_b128 v[222:225], v187 offset:40960
	ds_read_b128 v[226:229], v189 offset:32768
	v_exp_f32_e32 v107, v107
	v_add_f32_e32 v204, v103, v204
	v_exp_f32_e32 v108, v108
	v_add_f32_e32 v204, v104, v204
	v_exp_f32_e32 v109, v109
	v_add_f32_e32 v204, v105, v204
	s_waitcnt lgkmcnt(0)
	v_mfma_f32_32x32x64_f8f6f4 v[80:95], v[222:229], v[136:143], v[80:95]
	v_exp_f32_e32 v110, v110
	v_add_f32_e32 v204, v106, v204
	v_exp_f32_e32 v111, v111
	v_add_f32_e32 v204, v107, v204
	v_add_f32_e32 v204, v108, v204
	v_add_f32_e32 v204, v109, v204
	v_add_f32_e32 v204, v110, v204
	v_add_f32_e32 v204, v111, v204
	v_mov_b32_e32 v205, v204
	ds_read_b128 v[226:229], v192 offset:32768
	ds_read_b128 v[222:225], v191 offset:32768
	s_nop 1
	v_permlane32_swap_b32_e32 v204, v205
	v_cvt_pk_bf16_f32 v206, v112, v113
	v_cvt_pk_bf16_f32 v207, v114, v115
	v_cvt_pk_bf16_f32 v208, v116, v117
	v_cvt_pk_bf16_f32 v209, v118, v119
	v_cvt_pk_bf16_f32 v210, v120, v121
	v_cvt_pk_bf16_f32 v211, v122, v123
	s_waitcnt lgkmcnt(0)
	v_mfma_f32_32x32x64_f8f6f4 v[64:79], v[222:229], v[144:151], v[64:79]
	v_cvt_pk_bf16_f32 v212, v124, v125
	v_cvt_pk_bf16_f32 v213, v126, v127
	v_cvt_pk_bf16_f32 v214, v96, v97
	v_cvt_pk_bf16_f32 v215, v98, v99
	v_cvt_pk_bf16_f32 v216, v100, v101
	v_cvt_pk_bf16_f32 v217, v102, v103
	v_cvt_pk_bf16_f32 v218, v104, v105
	v_cvt_pk_bf16_f32 v219, v106, v107
	v_cvt_pk_bf16_f32 v220, v108, v109
	v_cvt_pk_bf16_f32 v221, v110, v111
	s_nop 0
	ds_read_b128 v[222:225], v191 offset:40960
	ds_read_b128 v[226:229], v193 offset:32768
	v_permlane32_swap_b32_e32 v206, v208
	v_permlane32_swap_b32_e32 v207, v209
	v_permlane32_swap_b32_e32 v210, v212
	v_permlane32_swap_b32_e32 v211, v213
	v_permlane32_swap_b32_e32 v214, v216
	s_waitcnt lgkmcnt(0)
	v_mfma_f32_32x32x64_f8f6f4 v[80:95], v[222:229], v[144:151], v[80:95]
	v_permlane32_swap_b32_e32 v215, v217
	v_permlane32_swap_b32_e32 v218, v220
	v_permlane32_swap_b32_e32 v219, v221
	ds_read_b64_tr_b16 v[222:223], v199 offset:0
	ds_read_b64_tr_b16 v[224:225], v199 offset:0x800
	ds_read_b64_tr_b16 v[226:227], v199 offset:0x1000
	ds_read_b64_tr_b16 v[228:229], v199 offset:0x1800
	ds_read_b64_tr_b16 v[230:231], v199 offset:0x2000
	ds_read_b64_tr_b16 v[232:233], v199 offset:0x2800
	ds_read_b64_tr_b16 v[234:235], v199 offset:0x3000
	ds_read_b64_tr_b16 v[236:237], v199 offset:0x3800
	v_max_f32_e32 v242, v65, v65
	v_max_f32_e32 v243, v64, v64
	v_max_f32_e32 v242, v243, v242
	v_max3_f32 v242, v242, v66, v67
	v_max3_f32 v242, v242, v68, v69
	v_max3_f32 v242, v242, v70, v71
	v_max3_f32 v242, v242, v72, v73
	v_max3_f32 v242, v242, v74, v75
	s_waitcnt lgkmcnt(0)
	s_nop 0
	v_mfma_f32_32x32x16_bf16 v[0:15], v[206:209], v[222:225], v[0:15]
	v_max3_f32 v242, v242, v76, v77
	v_max3_f32 v242, v242, v78, v79
	v_max3_f32 v242, v242, v80, v81
	v_max3_f32 v242, v242, v82, v83
	v_max3_f32 v242, v242, v84, v85
	ds_read_b64_tr_b16 v[222:223], v199 offset:0x200
	ds_read_b64_tr_b16 v[224:225], v199 offset:0xa00
	v_mfma_f32_32x32x16_bf16 v[0:15], v[210:213], v[226:229], v[0:15]
	v_max3_f32 v242, v242, v86, v87
	v_max3_f32 v242, v242, v88, v89
	v_max3_f32 v242, v242, v90, v91
	v_max3_f32 v242, v242, v92, v93
	v_max3_f32 v242, v242, v94, v95
	ds_read_b64_tr_b16 v[226:227], v199 offset:0x1200
	ds_read_b64_tr_b16 v[228:229], v199 offset:0x1a00
	v_mfma_f32_32x32x16_bf16 v[0:15], v[214:217], v[230:233], v[0:15]
	v_mov_b32_e32 v243, v242
	s_nop 1
	v_permlane32_swap_b32_e32 v242, v243
	ds_read_b64_tr_b16 v[230:231], v199 offset:0x2200
	ds_read_b64_tr_b16 v[232:233], v199 offset:0x2a00
	v_mfma_f32_32x32x16_bf16 v[0:15], v[218:221], v[234:237], v[0:15]
	v_max_f32_e32 v243, v243, v243
	v_max_f32_e32 v242, v242, v242
	v_max_f32_e32 v242, v242, v243
	v_sub_f32_e32 v243, v242, v195
	v_cmp_ge_f32_e32 vcc, s93, v243
	ds_read_b64_tr_b16 v[234:235], v199 offset:0x3200
	ds_read_b64_tr_b16 v[236:237], v199 offset:0x3a00
	v_max_f32_e32 v243, v195, v195
	v_max_f32_e32 v243, v243, v242
	v_sub_f32_e32 v242, v195, v243
	v_mul_f32_e32 v242, 0x3dd53b94, v242
	v_exp_f32_e32 v242, v242
	s_cmp_eq_u64 vcc, exec
	s_cselect_b64 s[6:7], -1, 0
	s_waitcnt lgkmcnt(0)
	v_mfma_f32_32x32x16_bf16 v[48:63], v[206:209], v[222:225], v[48:63]
	v_cndmask_b32_e64 v242, v242, 1.0, s[6:7]
	v_cmp_gt_f32_e32 vcc, 1.0, v242
	v_cndmask_b32_e64 v195, v243, v195, s[6:7]
	v_mul_f32_e32 v244, 0xbdd53b94, v195
	v_mov_b32_e32 v243, v244
	ds_read_b64_tr_b16 v[222:223], v199 offset:0x400
	ds_read_b64_tr_b16 v[224:225], v199 offset:0xc00
	v_mfma_f32_32x32x16_bf16 v[48:63], v[210:213], v[226:229], v[48:63]
	v_fmamk_f32 v64, v64, 0x3dd53b94, v244
	v_fmamk_f32 v65, v65, 0x3dd53b94, v244
	v_fmamk_f32 v66, v66, 0x3dd53b94, v244
	v_fmamk_f32 v67, v67, 0x3dd53b94, v244
	v_fmamk_f32 v68, v68, 0x3dd53b94, v244
	ds_read_b64_tr_b16 v[226:227], v199 offset:0x1400
	ds_read_b64_tr_b16 v[228:229], v199 offset:0x1c00
	v_mfma_f32_32x32x16_bf16 v[48:63], v[214:217], v[230:233], v[48:63]
	v_fmamk_f32 v69, v69, 0x3dd53b94, v244
	v_fmamk_f32 v70, v70, 0x3dd53b94, v244
	v_fmamk_f32 v71, v71, 0x3dd53b94, v244
	v_fmamk_f32 v72, v72, 0x3dd53b94, v244
	v_fmamk_f32 v73, v73, 0x3dd53b94, v244
	ds_read_b64_tr_b16 v[230:231], v199 offset:0x2400
	ds_read_b64_tr_b16 v[232:233], v199 offset:0x2c00
	v_mfma_f32_32x32x16_bf16 v[48:63], v[218:221], v[234:237], v[48:63]
	v_fmamk_f32 v74, v74, 0x3dd53b94, v244
	v_fmamk_f32 v75, v75, 0x3dd53b94, v244
	v_fmamk_f32 v76, v76, 0x3dd53b94, v244
	v_fmamk_f32 v77, v77, 0x3dd53b94, v244
	v_fmamk_f32 v78, v78, 0x3dd53b94, v244
	ds_read_b64_tr_b16 v[234:235], v199 offset:0x3400
	ds_read_b64_tr_b16 v[236:237], v199 offset:0x3c00
	v_fmac_f32_e32 v243, 0x3dd53b94, v79
	v_exp_f32_e32 v64, v64
	v_exp_f32_e32 v65, v65
	v_exp_f32_e32 v66, v66
	s_waitcnt lgkmcnt(0)
	v_mfma_f32_32x32x16_bf16 v[32:47], v[206:209], v[222:225], v[32:47]
	v_exp_f32_e32 v67, v67
	v_exp_f32_e32 v68, v68
	ds_read_b64_tr_b16 v[222:223], v199 offset:0x600
	ds_read_b64_tr_b16 v[224:225], v199 offset:0xe00
	v_mfma_f32_32x32x16_bf16 v[32:47], v[210:213], v[226:229], v[32:47]
	v_exp_f32_e32 v69, v69
	v_exp_f32_e32 v70, v70
	ds_read_b64_tr_b16 v[226:227], v199 offset:0x1600
	ds_read_b64_tr_b16 v[228:229], v199 offset:0x1e00
	v_mfma_f32_32x32x16_bf16 v[32:47], v[214:217], v[230:233], v[32:47]
	v_exp_f32_e32 v71, v71
	v_exp_f32_e32 v72, v72
	ds_read_b64_tr_b16 v[230:231], v199 offset:0x2600
	ds_read_b64_tr_b16 v[232:233], v199 offset:0x2e00
	v_mfma_f32_32x32x16_bf16 v[32:47], v[218:221], v[234:237], v[32:47]
	v_exp_f32_e32 v73, v73
	v_exp_f32_e32 v74, v74
	ds_read_b64_tr_b16 v[234:235], v199 offset:0x3600
	ds_read_b64_tr_b16 v[236:237], v199 offset:0x3e00
	v_exp_f32_e32 v75, v75
	v_exp_f32_e32 v76, v76
	v_exp_f32_e32 v77, v77
	v_exp_f32_e32 v78, v78
	s_waitcnt lgkmcnt(0)
	v_mfma_f32_32x32x16_bf16 v[16:31], v[206:209], v[222:225], v[16:31]
	v_exp_f32_e32 v79, v243
	v_pk_fma_f32 v[94:95], v[94:95], s[54:55], v[244:245] op_sel_hi:[1,0,0]
	v_mfma_f32_32x32x16_bf16 v[16:31], v[210:213], v[226:229], v[16:31]
	v_pk_fma_f32 v[92:93], v[92:93], s[54:55], v[244:245] op_sel_hi:[1,0,0]
	v_pk_fma_f32 v[90:91], v[90:91], s[54:55], v[244:245] op_sel_hi:[1,0,0]
	v_mfma_f32_32x32x16_bf16 v[16:31], v[214:217], v[230:233], v[16:31]
	v_pk_fma_f32 v[88:89], v[88:89], s[54:55], v[244:245] op_sel_hi:[1,0,0]
	v_pk_fma_f32 v[86:87], v[86:87], s[54:55], v[244:245] op_sel_hi:[1,0,0]
	v_mfma_f32_32x32x16_bf16 v[16:31], v[218:221], v[234:237], v[16:31]
	v_pk_fma_f32 v[84:85], v[84:85], s[54:55], v[244:245] op_sel_hi:[1,0,0]
	v_pk_fma_f32 v[82:83], v[82:83], s[54:55], v[244:245] op_sel_hi:[1,0,0]
	v_pk_fma_f32 v[80:81], v[80:81], s[54:55], v[244:245] op_sel_hi:[1,0,0]
	v_mov_b32_e32 v206, v242
	s_cbranch_vccz .Latt0_nrB
	s_nop 7
	s_nop 7
	s_and_saveexec_b64 s[38:39], s[4:5]
	ds_write_b32 v197, v206 offset:128
	s_or_b64 exec, exec, s[38:39]
	s_waitcnt lgkmcnt(0)
	v_add_u32_e32 v220, s77, v196
	ds_read_b128 v[208:211], v220 offset:224
	ds_read_b128 v[212:215], v220 offset:192
	ds_read_b128 v[216:219], v220 offset:160
	ds_read_b128 v[220:223], v220 offset:128
	s_waitcnt lgkmcnt(0)
	v_pk_mul_f32 v[12:13], v[12:13], v[208:209]
	v_pk_mul_f32 v[8:9], v[8:9], v[212:213]
	v_pk_mul_f32 v[4:5], v[4:5], v[216:217]
	v_pk_mul_f32 v[14:15], v[14:15], v[210:211]
	v_pk_mul_f32 v[10:11], v[10:11], v[214:215]
	v_pk_mul_f32 v[6:7], v[6:7], v[218:219]
	v_pk_mul_f32 v[2:3], v[2:3], v[222:223]
	v_pk_mul_f32 v[0:1], v[0:1], v[220:221]
	v_pk_mul_f32 v[60:61], v[60:61], v[208:209]
	v_pk_mul_f32 v[56:57], v[56:57], v[212:213]
	v_pk_mul_f32 v[52:53], v[52:53], v[216:217]
	v_pk_mul_f32 v[62:63], v[62:63], v[210:211]
	v_pk_mul_f32 v[58:59], v[58:59], v[214:215]
	v_pk_mul_f32 v[54:55], v[54:55], v[218:219]
	v_pk_mul_f32 v[50:51], v[50:51], v[222:223]
	v_pk_mul_f32 v[48:49], v[48:49], v[220:221]
	v_pk_mul_f32 v[44:45], v[44:45], v[208:209]
	v_pk_mul_f32 v[40:41], v[40:41], v[212:213]
	v_pk_mul_f32 v[36:37], v[36:37], v[216:217]
	v_pk_mul_f32 v[46:47], v[46:47], v[210:211]
	v_pk_mul_f32 v[42:43], v[42:43], v[214:215]
	v_pk_mul_f32 v[38:39], v[38:39], v[218:219]
	v_pk_mul_f32 v[34:35], v[34:35], v[222:223]
	v_pk_mul_f32 v[32:33], v[32:33], v[220:221]
	v_pk_mul_f32 v[28:29], v[28:29], v[208:209]
	v_pk_mul_f32 v[24:25], v[24:25], v[212:213]
	v_pk_mul_f32 v[20:21], v[20:21], v[216:217]
	v_pk_mul_f32 v[30:31], v[30:31], v[210:211]
	v_pk_mul_f32 v[26:27], v[26:27], v[214:215]
	v_pk_mul_f32 v[22:23], v[22:23], v[218:219]
	v_pk_mul_f32 v[18:19], v[18:19], v[222:223]
	v_pk_mul_f32 v[16:17], v[16:17], v[220:221]
.Latt0_nrB:
	s_branch .LBB0_520
